# best + P9 start stagger: 8 WG groups per XCD offset by 0.7us to de-synchronize epilogue store bursts
# baseline (speedup 1.0000x reference)
;     DI bool next(int i, Unit& u) const {
;         const long L = (long)i * G + c; if (L >= nwg) return false;
; __global__ void __launch_bounds__(NTHR, 2) mk_fwd(Args args) {
;     ...
;         __syncthreads();
;         const int NT = te[MAXRT];
;         if (IN(9)) { pg8::Gemm g{(const bf16*)(F.ws + WS_XN), (const bf16*)(F.ws + WS_WUP), DM / 2, (size_t)UPW * DM, (const int*)(F.ws + WS_SMALL + SM_ROWTOK), te, F.lds + MISC_OFF + 4096, F.lds + ESTASH_OFF};   pg8::StaticOrder S; S.init(NT, UPW / 256, F.G, (int)blockIdx.x);
.LBB0_1070:
	s_or_b64 exec, exec, s[0:1]
	s_add_i32 s0, 0, 0x20880
	v_mov_b32_e32 v1, s0
	s_waitcnt lgkmcnt(0)
	s_barrier
	ds_read_b32 v1, v1
	s_and_b64 vcc, exec, s[6:7]
	s_waitcnt lgkmcnt(0)
	v_readfirstlane_b32 s46, v1
	s_cbranch_vccz .LBB0_1095
	s_lshl_b32 s2, s46, 4
	s_cmp_ge_i32 s81, s2
	v_readfirstlane_b32 s3, v0
	s_cbranch_scc1 .LBB0_1095
	s_bfe_u32 s32, s81, 0x30003
	s_cmp_eq_u32 s32, 0
	s_cbranch_scc1 .Lstag9_done
.Lstag9_loop:
	s_sleep 23
	s_add_i32 s32, s32, -1
	s_cmp_lg_u32 s32, 0
	s_cbranch_scc1 .Lstag9_loop
;     DI bool next(int i, Unit& u) const {
;     ...
;         int wgid = (int)L; { const int q = nwg / NXCD, r = nwg % NXCD, xcd = wgid % NXCD, off = wgid / NXCD; wgid = (xcd < r ? xcd * (q + 1) : r * (q + 1) + (xcd - r) * q) + off; }
;         const int nig = WGM * nN, gid = wgid / nig, fm = gid * WGM, gsz = (nM - fm) < WGM ? (nM - fm) : WGM;
;         u.pm = fm + ((wgid % nig) % gsz); u.pn = (wgid % nig) / gsz; u.e = 0; return true;
;     }
; template <class Epi, bool GATHER, bool EXPERT, bool FP8>
; DI void gemm_phase(LAS unsigned char* lds, const Gemm g, const StaticOrder& S, const Epi& E) {
;     const int tid = threadIdx.x, wid = __builtin_amdgcn_readfirstlane(tid >> 6), lane = tid & 63, wr = wid >> 2, wc = wid & 3, fr = lane & 15, fq = lane >> 4;
;     const int K = g.K, nt = K / BK;
;     unsigned voffB[2], coffA[2][2];
;     const size_t kstep = (size_t)(BK * 2), hstep = (size_t)HALF * K * 2, tstep = 2 * hstep;
; #pragma unroll
;     for (int i = 0; i < 2; ++i) { int R, C; stage_rc(tid * 16 + i * 8192, R, C); const int Rb = Epi::PERM ? ((R & ~31) + perm32(R & 31)) : R;
;         voffB[i] = (unsigned)(Rb * K + C) * 2u; }
;     const unsigned ldsw = (unsigned)wid * 1024u;
;     const int aoff = lds_byte(wr * 64 + fr, fq * 8), boff = lds_byte(wc * 32 + fr, fq * 8);
;     ...
;     Unit cur, nxt; int ui = 0;
;     if (!S.next(0, cur)) return;
;     if (EXPERT) cur.e = __builtin_amdgcn_readfirstlane(g.tile_e[cur.pm]);
;     f32x4 acc[2][2][4][2];
; #pragma unroll
;     for (int a = 0; a < 2; ++a)
; #pragma unroll
;         for (int b = 0; b < 2; ++b)
; #pragma unroll
;             for (int m = 0; m < 4; ++m)
; #pragma unroll
;                 for (int n = 0; n < 2; ++n) acc[a][b][m][n] = (f32x4){0.f, 0.f, 0.f, 0.f};
;     bf16x8 At[4][2], B0[2][2], B1[2][2];
;     PG8_OFFS(coffA, cur.pm);
;     const char* cA = sptr((const char*)g.A + (GATHER ? (size_t)0 : (size_t)cur.pm * tstep));
;     const char* cB = sptr((const char*)g.Bt + (size_t)cur.e * g.estride + (size_t)cur.pn * tstep);
;     LAS unsigned char* est = g.estash + wid * 768;
;     if (Epi::STASH) E.prefetch(cur, wr, wc, lane, est);
;     LAS unsigned char* stash = g.stash + wid * 256;
;     PG8_STAGE_B(PG8_SB(0, 0), cB); PG8_STAGE_B(PG8_SB(0, 1), cB + hstep); PG8_STAGE_A(PG8_SA(0, 0), cA, coffA[0][0], coffA[0][1]); PG8_STAGE_A(PG8_SA(0, 1), cA, coffA[1][0], coffA[1][1]);
;     if (wr == 1) PG8_BAR;
.Lstag9_done:
	s_add_u32 s8, s94, 0x34000000
	s_addc_u32 s9, s95, 0
	s_add_u32 s80, s94, 0x4000000
	s_addc_u32 s44, s95, 0
	s_add_u32 s10, s94, 0x26a3000
	s_addc_u32 s11, s95, 0
	s_add_u32 s4, s94, 0x27d4000
	s_addc_u32 s5, s95, 0
	s_ashr_i32 s49, s81, 31
	s_lshr_b32 s0, s49, 29
	s_add_i32 s0, s81, s0
	s_lshr_b32 s16, s3, 6
	s_lshr_b32 s19, s3, 8
	s_lshl_b32 s48, s46, 1
	s_ashr_i32 s1, s0, 3
	s_and_b32 s0, s0, -8
	s_bfe_u32 s18, s3, 0x20006
	s_lshl_b32 s45, s16, 10
	s_lshl_b32 s47, s19, 6
	s_sub_i32 s0, s81, s0
	s_or_b32 s50, s48, 1
	s_cmp_lt_i32 s0, 0
	s_cselect_b32 s12, s50, s48
	s_mul_i32 s0, s12, s0
	s_add_i32 s0, s0, s1
	s_ashr_i32 s1, s0, 31
	s_lshr_b32 s1, s1, 25
	s_add_i32 s1, s0, s1
	s_ashr_i32 s12, s1, 7
	s_lshl_b32 s12, s12, 3
	s_sub_i32 s13, s46, s12
	s_min_i32 s13, s13, 8
	s_abs_i32 s14, s13
	v_cvt_f32_u32_e32 v1, s14
	s_sub_i32 s17, 0, s14
	s_and_b32 s1, s1, 0xffffff80
	s_sub_i32 s0, s0, s1
	v_rcp_iflag_f32_e32 v1, v1
	s_abs_i32 s15, s0
	s_xor_b32 s1, s0, s13
	s_ashr_i32 s1, s1, 31
	v_mul_f32_e32 v1, 0x4f7ffffe, v1
	v_cvt_u32_f32_e32 v1, v1
	v_lshlrev_b32_e32 v146, 2, v224
	s_waitcnt vmcnt(16)
	v_mov_b32_e32 v147, 0
	s_mov_b32 s56, 0
	v_readfirstlane_b32 s20, v1
	s_mul_i32 s17, s17, s20
	s_mul_hi_u32 s17, s20, s17
	s_add_i32 s20, s20, s17
	s_mul_hi_u32 s17, s15, s20
	s_mul_i32 s20, s17, s14
	s_sub_i32 s15, s15, s20
	s_add_i32 s20, s17, 1
	s_sub_i32 s21, s15, s14
	s_cmp_ge_u32 s15, s14
	s_cselect_b32 s17, s20, s17
	s_cselect_b32 s15, s21, s15
	s_add_i32 s20, s17, 1
	s_cmp_ge_u32 s15, s14
	s_cselect_b32 s14, s20, s17
	s_xor_b32 s14, s14, s1
	s_sub_i32 s34, s14, s1
	s_mul_i32 s1, s34, s13
	s_sub_i32 s0, s0, s1
	s_add_i32 s33, s12, s0
	s_lshl_b32 s0, s33, 2
	s_add_i32 s0, s0, 0
	s_add_i32 s0, s0, 0x20000
	v_mov_b32_e32 v1, s0
	ds_read_b32 v10, v1
	v_mov_b32_e32 v1, v0
	s_lshl_b32 s0, s33, 8
	v_ashrrev_i32_e32 v2, 31, v1
	v_lshrrev_b32_e32 v2, 26, v2
	v_lshlrev_b32_e32 v6, 4, v1
	v_add_u32_e32 v2, v1, v2
	v_bfe_i32 v1, v1, 27, 1
	v_lshrrev_b32_e32 v1, 22, v1
	v_add_u32_e32 v1, v6, v1
	v_and_b32_e32 v1, 0xfffffc00, v1
	v_sub_u32_e32 v1, v6, v1
	v_ashrrev_i32_e32 v11, 6, v2
	v_lshrrev_b32_e32 v2, 4, v1
	v_bitop3_b32 v12, v2, v1, 32 bitop3:0x6c
	v_ashrrev_i32_e32 v2, 31, v12
	v_lshrrev_b32_e32 v2, 26, v2
	v_lshlrev_b32_e32 v1, 3, v11
	v_add_u32_e32 v13, v12, v2
	v_and_b32_e32 v1, -16, v1
	v_ashrrev_i32_e32 v2, 6, v13
	v_add3_u32 v2, v1, s0, v2
	v_add_u32_e32 v1, 0x2000, v6
	v_ashrrev_i32_e32 v6, 31, v1
	v_lshrrev_b32_e32 v6, 22, v6
	v_add_u32_e32 v6, v1, v6
	v_ashrrev_i32_e32 v14, 10, v6
	v_mul_i32_i24_e32 v6, 0x400, v14
	v_sub_u32_e32 v1, v1, v6
	v_lshrrev_b32_e32 v6, 4, v1
	v_bitop3_b32 v15, v6, v1, 32 bitop3:0x6c
	v_ashrrev_i32_e32 v6, 31, v15
	v_lshrrev_b32_e32 v6, 26, v6
	v_lshlrev_b32_e32 v1, 3, v14
	v_add_u32_e32 v16, v15, v6
	v_and_b32_e32 v1, -16, v1
	v_ashrrev_i32_e32 v6, 6, v16
	v_add3_u32 v6, v1, s0, v6
	v_ashrrev_i32_e32 v3, 31, v2
	v_ashrrev_i32_e32 v7, 31, v6
	v_lshl_add_u64 v[4:5], v[2:3], 2, s[10:11]
	v_add_u32_e32 v2, 0x80, v2
	v_lshl_add_u64 v[8:9], v[6:7], 2, s[10:11]
	v_add_u32_e32 v6, 0x80, v6
	v_ashrrev_i32_e32 v3, 31, v2
	v_ashrrev_i32_e32 v7, 31, v6
	v_lshl_add_u64 v[2:3], v[2:3], 2, s[10:11]
	v_lshl_add_u64 v[6:7], v[6:7], 2, s[10:11]
	global_load_dword v17, v[4:5], off
	global_load_dword v18, v[2:3], off
	global_load_dword v19, v[8:9], off
	global_load_dword v20, v[6:7], off
	s_waitcnt lgkmcnt(0)
	v_readfirstlane_b32 s14, v10
	v_lshlrev_b32_e32 v2, 4, v0
	v_and_b32_e32 v3, 32, v0
	v_lshrrev_b32_e32 v4, 1, v0
	v_bfe_u32 v5, v0, 2, 2
	v_lshrrev_b32_e32 v6, 3, v0
	v_lshrrev_b32_e32 v8, 5, v0
	s_ashr_i32 s15, s14, 31
	s_movk_i32 s1, 0x60
	v_bitop3_b32 v2, v2, v3, 48 bitop3:0x6c
	v_and_or_b32 v3, v4, 24, v5
	v_and_b32_e32 v4, 32, v6
	v_and_b32_e32 v5, 4, v8
	s_lshl_b64 s[12:13], s[14:15], 23
	v_bitop3_b32 v6, v6, s1, 64 bitop3:0xc8
	v_or3_b32 v4, v5, v4, v3
	s_add_u32 s1, s80, s12
	v_and_b32_e32 v7, 64, v0
	v_lshlrev_b32_e32 v4, 11, v4
	s_addc_u32 s17, s44, s13
	s_ashr_i32 s35, s34, 31
	v_or3_b32 v3, v5, v6, v3
	v_or3_b32 v158, v4, v7, v2
	v_and_b32_e32 v4, 0xc0, v13
	s_lshl_b64 s[12:13], s[34:35], 19
	v_mov_b32_e32 v1, 1
	v_lshlrev_b32_e32 v3, 11, v3
	v_sub_u32_e32 v4, v12, v4
	s_add_u32 s36, s1, s12
	s_mul_i32 s1, s16, 0x300
	v_or3_b32 v159, v3, v7, v2
	v_lshlrev_b32_e32 v2, 5, v11
	v_ashrrev_i16_sdwa v4, v1, sext(v4) dst_sel:DWORD dst_unused:UNUSED_PAD src0_sel:DWORD src1_sel:BYTE_0
	s_addc_u32 s37, s17, s13
	s_add_i32 s17, s1, 0
	s_ashr_i32 s1, s0, 31
	v_and_b32_e32 v2, 32, v2
	v_bfe_i32 v4, v4, 0, 16
	v_and_b32_e32 v5, 0xc0, v16
	s_add_i32 s35, s17, 0x24000
	s_lshl_b64 s[0:1], s[0:1], 2
	v_add_lshl_u32 v2, v2, v4, 1
	v_sub_u32_e32 v4, v15, v5
	s_add_u32 s0, s4, s0
	v_lshlrev_b32_e32 v3, 5, v14
	v_ashrrev_i16_sdwa v4, v1, sext(v4) dst_sel:DWORD dst_unused:UNUSED_PAD src0_sel:DWORD src1_sel:BYTE_0
	s_addc_u32 s1, s5, s1
	s_and_b32 s12, s3, 0xffffff00
	v_and_b32_e32 v3, 32, v3
	v_bfe_i32 v4, v4, 0, 16
	s_add_u32 s0, s0, s12
	v_add_lshl_u32 v3, v3, v4, 1
	s_addc_u32 s1, s1, 0
	s_mov_b32 m0, s35
	s_mov_b64 s[12:13], 0x200
	global_load_lds_dword v146, s[0:1]
	s_add_i32 m0, s17, 0x24100
	s_waitcnt vmcnt(0)
	v_lshl_add_u32 v162, v17, 11, v2
	v_lshl_add_u32 v160, v18, 11, v2
	v_lshl_add_u32 v163, v19, 11, v3
	v_lshl_add_u32 v161, v20, 11, v3
	v_lshl_add_u64 v[2:3], s[0:1], 0, v[146:147]
	s_lshl_b64 s[0:1], s[14:15], 14
	s_add_u32 s14, s54, s0
	s_addc_u32 s15, s55, s1
	s_lshl_b32 s0, s34, 8
	s_lshl_b32 s51, s18, 6
	s_or_b32 s0, s0, s51
	s_ashr_i32 s1, s0, 31
	s_lshl_b64 s[0:1], s[0:1], 2
	v_lshl_add_u64 v[2:3], v[2:3], 0, s[12:13]
	s_add_u32 s0, s14, s0
	global_load_lds_dword v[2:3], off
	s_addc_u32 s1, s15, s1
	s_add_i32 m0, s17, 0x24200
	v_mov_b32_e32 v2, v158
	s_add_i32 s52, s45, 0
	global_load_lds_dword v146, s[0:1]
	s_add_i32 m0, s52, 0x10000
	s_nop 0
	global_load_lds_dwordx4 v2, s[36:37]
	v_mov_b32_e32 v2, v159
	s_add_i32 m0, s52, 0x12000
	s_add_u32 s0, s36, 0x40000
	global_load_lds_dwordx4 v2, s[36:37]
	v_mov_b32_e32 v2, v158
	s_addc_u32 s1, s37, 0
	s_add_i32 m0, s52, 0x14000
	s_add_i32 s53, s52, 0x2000
	global_load_lds_dwordx4 v2, s[0:1]
	v_mov_b32_e32 v2, v159
	s_add_i32 m0, s52, 0x16000
	s_add_i32 s54, s52, 0x4000
	global_load_lds_dwordx4 v2, s[0:1]
	v_mov_b32_e32 v2, v162
	s_mov_b32 m0, s52
	s_add_i32 s55, s52, 0x6000
	global_load_lds_dwordx4 v2, s[8:9]
	v_mov_b32_e32 v2, v163
	s_mov_b32 m0, s53
	s_cmp_eq_u32 s19, 1
	global_load_lds_dwordx4 v2, s[8:9]
	v_mov_b32_e32 v2, v160
	s_mov_b32 m0, s54
	s_cselect_b64 s[14:15], -1, 0
	global_load_lds_dwordx4 v2, s[8:9]
	v_mov_b32_e32 v2, v161
	s_mov_b32 m0, s55
	s_cmp_lg_u32 s19, 1
	global_load_lds_dwordx4 v2, s[8:9]
	s_cbranch_scc1 .LBB0_1074
	s_barrier
